# PEER U: token start loads the next activation row straight into its home registers behind a counted wait; first-half row waits count the prefetched batch (vmcnt 31..16) and the second half waits vmcnt
# speedup vs baseline: 1.0082x; 1.0053x over previous
.Lpu_go1:
.LBB0_1737:
	s_cmp_lg_u32 s48, s56
	s_cbranch_scc1 .LBB0_1741
	s_cmp_gt_i32 s59, 15
	s_cbranch_scc1 .Lunx_drain
	s_waitcnt vmcnt(16)
	s_branch .Lunx_go

.LBB0_1741:
	s_waitcnt vmcnt(31)
	v_mfma_f32_16x16x32_fp8_fp8 v[164:167], v[72:73], v[148:149], 0
	v_mfma_f32_16x16x32_fp8_fp8 v[164:167], v[74:75], v[146:147], v[164:167]
	s_lshl_b32 s30, s58, 9
	v_lshl_add_u32 v136, s48, 4, v152
	s_add_i32 s30, s15, s30
	s_waitcnt vmcnt(30)
	v_mfma_f32_16x16x32_fp8_fp8 v[154:157], v[76:77], v[148:149], 0
	v_mfma_f32_16x16x32_fp8_fp8 v[154:157], v[78:79], v[146:147], v[154:157]
	s_waitcnt vmcnt(29)
	v_mfma_f32_16x16x32_fp8_fp8 v[168:171], v[80:81], v[148:149], 0
	v_mfma_f32_16x16x32_fp8_fp8 v[168:171], v[82:83], v[146:147], v[168:171]
	v_pk_mul_f32 v[172:173], v[164:165], v[174:175]
	v_pk_fma_f32 v[172:173], v[166:167], v[176:177], v[172:173]
	v_add_f32_e32 v137, v172, v173
	s_waitcnt vmcnt(28)
	v_mfma_f32_16x16x32_fp8_fp8 v[164:167], v[84:85], v[148:149], 0
	v_mfma_f32_16x16x32_fp8_fp8 v[164:167], v[86:87], v[146:147], v[164:167]
	v_pk_mul_f32 v[172:173], v[154:155], v[174:175]
	v_pk_fma_f32 v[172:173], v[156:157], v[176:177], v[172:173]
	v_add_f32_e32 v138, v172, v173
	s_waitcnt vmcnt(27)
	v_mfma_f32_16x16x32_fp8_fp8 v[154:157], v[88:89], v[148:149], 0
	v_mfma_f32_16x16x32_fp8_fp8 v[154:157], v[90:91], v[146:147], v[154:157]
	v_pk_mul_f32 v[172:173], v[168:169], v[174:175]
	v_pk_fma_f32 v[172:173], v[170:171], v[176:177], v[172:173]
	v_add_f32_e32 v139, v172, v173
	s_waitcnt vmcnt(26)
	v_mfma_f32_16x16x32_fp8_fp8 v[168:171], v[92:93], v[148:149], 0
	v_mfma_f32_16x16x32_fp8_fp8 v[168:171], v[94:95], v[146:147], v[168:171]
	v_pk_mul_f32 v[172:173], v[164:165], v[174:175]
	v_pk_fma_f32 v[172:173], v[166:167], v[176:177], v[172:173]
	v_add_f32_e32 v158, v172, v173
	s_waitcnt vmcnt(25)
	v_mfma_f32_16x16x32_fp8_fp8 v[164:167], v[96:97], v[148:149], 0
	v_mfma_f32_16x16x32_fp8_fp8 v[164:167], v[98:99], v[146:147], v[164:167]
	v_pk_mul_f32 v[172:173], v[154:155], v[174:175]
	v_pk_fma_f32 v[172:173], v[156:157], v[176:177], v[172:173]
	v_add_f32_e32 v159, v172, v173
	s_waitcnt vmcnt(24)
	v_mfma_f32_16x16x32_fp8_fp8 v[154:157], v[100:101], v[148:149], 0
	v_mfma_f32_16x16x32_fp8_fp8 v[154:157], v[102:103], v[146:147], v[154:157]
	v_pk_mul_f32 v[172:173], v[168:169], v[174:175]
	v_pk_fma_f32 v[172:173], v[170:171], v[176:177], v[172:173]
	v_add_f32_e32 v160, v172, v173
	v_pk_mul_f32 v[172:173], v[164:165], v[174:175]
	v_pk_fma_f32 v[172:173], v[166:167], v[176:177], v[172:173]
	v_add_f32_e32 v161, v172, v173
	s_nop 1
	v_pk_mul_f32 v[172:173], v[154:155], v[174:175]
	v_pk_fma_f32 v[172:173], v[156:157], v[176:177], v[172:173]
	v_add_f32_e32 v162, v172, v173
	v_permlane32_swap_b32_e32 v137, v159
	v_add_f32_e32 v137, v137, v159
	v_permlane32_swap_b32_e32 v138, v160
	v_add_f32_e32 v138, v138, v160
	v_permlane32_swap_b32_e32 v139, v161
	v_add_f32_e32 v139, v139, v161
	v_permlane32_swap_b32_e32 v158, v162
	v_add_f32_e32 v158, v158, v162
	v_permlane16_swap_b32_e32 v137, v139
	v_add_f32_e32 v137, v137, v139
	v_permlane16_swap_b32_e32 v138, v158
	v_add_f32_e32 v138, v138, v158
	v_add_f32_dpp v137, v137, v137 row_ror:8 row_mask:0xf bank_mask:0xf bound_ctrl:1
	s_nop 0
	v_add_f32_dpp v138, v138, v138 row_ror:8 row_mask:0xf bank_mask:0xf bound_ctrl:1
	v_add_f32_dpp v137, v137, v137 row_ror:4 row_mask:0xf bank_mask:0xf bound_ctrl:1
	s_nop 0
	v_add_f32_dpp v138, v138, v138 row_ror:4 row_mask:0xf bank_mask:0xf bound_ctrl:1
	v_add_f32_dpp v137, v137, v137 row_ror:2 row_mask:0xf bank_mask:0xf bound_ctrl:1
	s_nop 0
	v_add_f32_dpp v138, v138, v138 row_ror:2 row_mask:0xf bank_mask:0xf bound_ctrl:1
	v_add_f32_dpp v172, v137, v137 row_ror:1 row_mask:0xf bank_mask:0xf bound_ctrl:1
	s_nop 0
	v_add_f32_dpp v173, v138, v138 row_ror:1 row_mask:0xf bank_mask:0xf bound_ctrl:1
	v_lshl_add_u32 v137, v136, 2, s30
	s_lshl_b32 s72, s48, 4
	s_cmp_ge_i32 s72, s70
	s_cselect_b32 s73, 1, 0
	s_cmp_lt_i32 s72, s61
	s_cselect_b32 s72, 1, 0
	s_and_b32 s72, s72, s73
	s_cbranch_scc0 .Lug_h1g0_skip
	s_and_saveexec_b64 s[56:57], s[44:45]
	ds_read_b64 v[160:161], v137
	v_pk_mul_f32 v[172:173], v[172:173], v[178:179] op_sel_hi:[1,0]
	v_pk_mul_f32 v[158:159], v[172:173], v[178:179] op_sel:[0,1] op_sel_hi:[1,1]
	v_pk_mul_f32 v[158:159], v[172:173], v[158:159]
	v_pk_fma_f32 v[158:159], v[172:173], v[158:159], v[172:173]
	v_pk_mul_f32 v[158:159], v[158:159], v[180:181] op_sel_hi:[1,0]
	v_pk_mul_f32 v[158:159], v[158:159], v[180:181] op_sel:[0,1] op_sel_hi:[1,1]
	v_exp_f32_e32 v158, v158
	v_exp_f32_e32 v159, v159
	s_nop 0
	v_pk_add_f32 v[158:159], v[158:159], v[182:183] op_sel:[0,1] op_sel_hi:[1,1]
	v_rcp_f32_e32 v158, v158
	v_rcp_f32_e32 v159, v159
	s_nop 0
	v_pk_mul_f32 v[172:173], v[172:173], v[158:159]
	v_pk_mul_f32 v[172:173], v[172:173], v[182:183] op_sel_hi:[1,0]
	s_waitcnt lgkmcnt(0)
	v_pk_mul_f32 v[172:173], v[172:173], v[160:161]
	ds_write_b64 v137, v[172:173]
	s_or_b64 exec, exec, s[56:57]
.Lug_h1g0_skip:
	s_waitcnt vmcnt(23)
	v_mfma_f32_16x16x32_fp8_fp8 v[164:167], v[104:105], v[148:149], 0
	v_mfma_f32_16x16x32_fp8_fp8 v[164:167], v[106:107], v[146:147], v[164:167]
	s_waitcnt vmcnt(22)
	v_mfma_f32_16x16x32_fp8_fp8 v[154:157], v[108:109], v[148:149], 0
	v_mfma_f32_16x16x32_fp8_fp8 v[154:157], v[110:111], v[146:147], v[154:157]
	s_waitcnt vmcnt(21)
	v_mfma_f32_16x16x32_fp8_fp8 v[168:171], v[112:113], v[148:149], 0
	v_mfma_f32_16x16x32_fp8_fp8 v[168:171], v[114:115], v[146:147], v[168:171]
	s_nop 1
	v_pk_mul_f32 v[172:173], v[164:165], v[174:175]
	v_pk_fma_f32 v[172:173], v[166:167], v[176:177], v[172:173]
	v_add_f32_e32 v138, v172, v173
	s_waitcnt vmcnt(20)
	v_mfma_f32_16x16x32_fp8_fp8 v[164:167], v[116:117], v[148:149], 0
	v_mfma_f32_16x16x32_fp8_fp8 v[164:167], v[118:119], v[146:147], v[164:167]
	v_pk_mul_f32 v[172:173], v[154:155], v[174:175]
	v_pk_fma_f32 v[172:173], v[156:157], v[176:177], v[172:173]
	v_add_f32_e32 v139, v172, v173
	s_waitcnt vmcnt(19)
	v_mfma_f32_16x16x32_fp8_fp8 v[154:157], v[120:121], v[148:149], 0
	v_mfma_f32_16x16x32_fp8_fp8 v[154:157], v[122:123], v[146:147], v[154:157]
	v_pk_mul_f32 v[172:173], v[168:169], v[174:175]
	v_pk_fma_f32 v[172:173], v[170:171], v[176:177], v[172:173]
	v_add_f32_e32 v158, v172, v173
	s_waitcnt vmcnt(18)
	v_mfma_f32_16x16x32_fp8_fp8 v[168:171], v[124:125], v[148:149], 0
	v_mfma_f32_16x16x32_fp8_fp8 v[168:171], v[126:127], v[146:147], v[168:171]
	v_pk_mul_f32 v[172:173], v[164:165], v[174:175]
	v_pk_fma_f32 v[172:173], v[166:167], v[176:177], v[172:173]
	v_add_f32_e32 v159, v172, v173
	s_waitcnt vmcnt(17)
	v_mfma_f32_16x16x32_fp8_fp8 v[164:167], v[128:129], v[148:149], 0
	v_mfma_f32_16x16x32_fp8_fp8 v[164:167], v[130:131], v[146:147], v[164:167]
	v_pk_mul_f32 v[172:173], v[154:155], v[174:175]
	v_pk_fma_f32 v[172:173], v[156:157], v[176:177], v[172:173]
	v_add_f32_e32 v160, v172, v173
	s_waitcnt vmcnt(16)
	v_mfma_f32_16x16x32_fp8_fp8 v[154:157], v[132:133], v[148:149], 0
	v_mfma_f32_16x16x32_fp8_fp8 v[154:157], v[134:135], v[146:147], v[154:157]
	v_pk_mul_f32 v[172:173], v[168:169], v[174:175]
	v_pk_fma_f32 v[172:173], v[170:171], v[176:177], v[172:173]
	v_add_f32_e32 v161, v172, v173
	v_pk_mul_f32 v[172:173], v[164:165], v[174:175]
	v_pk_fma_f32 v[172:173], v[166:167], v[176:177], v[172:173]
	v_add_f32_e32 v162, v172, v173
	s_nop 1
	v_pk_mul_f32 v[172:173], v[154:155], v[174:175]
	v_pk_fma_f32 v[172:173], v[156:157], v[176:177], v[172:173]
	v_add_f32_e32 v163, v172, v173
	v_permlane32_swap_b32_e32 v138, v160
	v_add_f32_e32 v138, v138, v160
	v_permlane32_swap_b32_e32 v139, v161
	v_add_f32_e32 v139, v139, v161
	v_permlane32_swap_b32_e32 v158, v162
	v_add_f32_e32 v158, v158, v162
	v_permlane32_swap_b32_e32 v159, v163
	v_add_f32_e32 v159, v159, v163
	v_permlane16_swap_b32_e32 v138, v158
	v_add_f32_e32 v138, v138, v158
	v_permlane16_swap_b32_e32 v139, v159
	v_add_f32_e32 v139, v139, v159
	v_add_f32_dpp v138, v138, v138 row_ror:8 row_mask:0xf bank_mask:0xf bound_ctrl:1
	s_nop 0
	v_add_f32_dpp v139, v139, v139 row_ror:8 row_mask:0xf bank_mask:0xf bound_ctrl:1
	v_add_f32_dpp v138, v138, v138 row_ror:4 row_mask:0xf bank_mask:0xf bound_ctrl:1
	s_nop 0
	v_add_f32_dpp v139, v139, v139 row_ror:4 row_mask:0xf bank_mask:0xf bound_ctrl:1
	v_add_f32_dpp v138, v138, v138 row_ror:2 row_mask:0xf bank_mask:0xf bound_ctrl:1
	s_nop 0
	v_add_f32_dpp v139, v139, v139 row_ror:2 row_mask:0xf bank_mask:0xf bound_ctrl:1
	v_add_f32_dpp v172, v138, v138 row_ror:1 row_mask:0xf bank_mask:0xf bound_ctrl:1
	s_nop 0
	v_add_f32_dpp v173, v139, v139 row_ror:1 row_mask:0xf bank_mask:0xf bound_ctrl:1
	s_lshl_b32 s72, s48, 4
	s_cmp_ge_i32 s72, s70
	s_cselect_b32 s73, 1, 0
	s_cmp_lt_i32 s72, s61
	s_cselect_b32 s72, 1, 0
	s_and_b32 s72, s72, s73
	s_cbranch_scc0 .Lug_h1g1_skip
	s_and_saveexec_b64 s[56:57], s[44:45]
	ds_read_b64 v[160:161], v137 offset:32
	v_pk_mul_f32 v[172:173], v[172:173], v[178:179] op_sel_hi:[1,0]
	v_pk_mul_f32 v[158:159], v[172:173], v[178:179] op_sel:[0,1] op_sel_hi:[1,1]
	v_pk_mul_f32 v[158:159], v[172:173], v[158:159]
	v_pk_fma_f32 v[158:159], v[172:173], v[158:159], v[172:173]
	v_pk_mul_f32 v[158:159], v[158:159], v[180:181] op_sel_hi:[1,0]
	v_pk_mul_f32 v[158:159], v[158:159], v[180:181] op_sel:[0,1] op_sel_hi:[1,1]
	v_exp_f32_e32 v158, v158
	v_exp_f32_e32 v159, v159
	s_nop 0
	v_pk_add_f32 v[158:159], v[158:159], v[182:183] op_sel:[0,1] op_sel_hi:[1,1]
	v_rcp_f32_e32 v158, v158
	v_rcp_f32_e32 v159, v159
	s_nop 0
	v_pk_mul_f32 v[172:173], v[172:173], v[158:159]
	v_pk_mul_f32 v[172:173], v[172:173], v[182:183] op_sel_hi:[1,0]
	s_waitcnt lgkmcnt(0)
	v_pk_mul_f32 v[172:173], v[172:173], v[160:161]
	ds_write_b64 v137, v[172:173] offset:32
	s_or_b64 exec, exec, s[56:57]
